# strategy 2 (7.3): L1 epilogue 8 narrow stores -> 3 dwordx4 via W-row permutation at LDS staging; bias reads batched
# speedup vs baseline: 1.0054x; 1.0054x over previous
_Z7k_layerILi1EEvPKDF16_PKiPKjS3_S3_S1_PKfPDF16_PhS3_S7_Pf:
	s_load_dwordx2 s[24:25], s[0:1], 0x50
	s_load_dwordx8 s[8:15], s[0:1], 0x0
	s_load_dwordx8 s[16:23], s[0:1], 0x20
	v_lshrrev_b32_e32 v2, 5, v0
	v_and_b32_e32 v4, 31, v0
	v_bfe_u32 v3, v2, 2, 2
	v_lshrrev_b32_e32 v6, 4, v2
	v_and_b32_e32 v7, 3, v2
	v_lshl_add_u32 v3, v3, 4, v7
	v_lshl_add_u32 v3, v6, 2, v3
	v_mul_u32_u24_e32 v3, 0x220, v3
	v_lshlrev_b32_e32 v5, 4, v4
	v_or_b32_e32 v1, 0xfffffc00, v0
	v_add3_u32 v4, v3, v5, 0
	v_add_u32_e32 v4, 0x1cd90, v4
	v_lshl_or_b32 v2, v2, 9, v5
	v_mov_b32_e32 v3, 0
	s_waitcnt lgkmcnt(0)
	v_add_u32_e32 v3, 0x4000, v2
	v_lshlrev_b32_e32 v30, 4, v0
	v_cmp_gt_u32_e64 s[34:35], 16, v0
	v_lshrrev_b32_e32 v39, 6, v0
	s_and_saveexec_b64 s[4:5], s[34:35]
	global_load_dwordx4 v[42:45], v30, s[20:21]
	s_mov_b64 exec, s[4:5]
	global_load_dwordx4 v[6:9], v2, s[18:19]
	global_load_dwordx4 v[10:13], v3, s[18:19]
	v_add_u32_e32 v31, 0x4000, v30
	v_add_u32_e32 v32, 0x8000, v30
	v_add_u32_e32 v33, 0xc000, v30
	global_load_dwordx4 v[14:17], v30, s[8:9]
	global_load_dwordx4 v[18:21], v31, s[8:9]
	global_load_dwordx4 v[22:25], v32, s[8:9]
	global_load_dwordx4 v[26:29], v33, s[8:9]
	v_readfirstlane_b32 s36, v39
	v_mov_b32_e32 v40, v4
	v_add_u32_e32 v41, 0xcc10, v30
	v_add_u32_e32 v38, 0x1cc90, v30
	v_cmp_gt_u32_e32 vcc, 64, v0
	s_and_saveexec_b64 s[4:5], vcc
	v_lshl_add_u32 v1, v0, 1, 0
	v_add_u32_e32 v1, 0x1cc10, v1
	v_mov_b32_e32 v2, 0
	ds_write_b16 v1, v2
	s_mov_b64 exec, s[4:5]
	v_cmp_eq_u32_e32 vcc, 0, v0
	s_and_saveexec_b64 s[4:5], vcc
	v_mov_b32_e32 v1, 0
	v_mov_b32_e32 v2, 16
	ds_write_b32 v1, v2 offset:52224
	s_mov_b64 exec, s[4:5]
	s_mul_i32 s8, s2, 0x186a0
	s_lshr_b32 s8, s8, 8
	s_add_i32 s3, s2, 1
	s_mul_i32 s18, s3, 0x186a0
	s_lshr_b32 s18, s18, 8
.LBB4_14:
	v_lshrrev_b32_e32 v2, 3, v0
	s_load_dwordx2 s[4:5], s[0:1], 0x40
	v_and_b32_e32 v2, 0x78, v2
	s_movk_i32 s2, 0xa0
	v_and_b32_e32 v97, 7, v0
	s_sub_i32 s0, s18, s8
	v_and_b32_e32 v1, 63, v0
	v_mov_b32_e32 v89, 0
	v_mad_u32_u24 v3, v2, s2, 0
	v_bfe_u32 v96, v0, 3, 3
	v_and_b32_e32 v99, 15, v0
	v_bfe_u32 v4, v0, 4, 2
	s_add_i32 s0, s0, 7
	v_mul_u32_u24_e32 v5, 0xa0, v97
	v_and_b32_e32 v0, 48, v0
	s_ashr_i32 s9, s0, 3
	v_cmp_eq_u32_e64 s[0:1], 0, v1
	v_mad_u32_u24 v1, v96, s2, v3
	v_lshlrev_b32_e32 v2, 5, v4
	v_add3_u32 v103, v3, v5, v0
	v_mov_b32_e32 v3, v89
	v_lshlrev_b32_e32 v98, 4, v97
	v_add_u32_e32 v0, 0, v0
	v_lshlrev_b32_e32 v88, 4, v4
	v_lshl_add_u64 v[90:91], s[22:23], 0, v[2:3]
	v_mul_u32_u24_e32 v2, 0x220, v99
	v_or_b32_e32 v100, 8, v97
	v_or_b32_e32 v101, 16, v97
	v_add_u32_e32 v102, 0, v98
	v_cmp_gt_u32_e64 s[2:3], 8, v99
	s_waitcnt lgkmcnt(0)
	v_lshl_add_u64 v[92:93], s[4:5], 0, v[88:89]
	v_lshlrev_b32_e32 v88, 2, v88
	v_add_u32_e32 v104, v1, v98
	v_add_u32_e32 v105, v0, v2
	v_add_u32_e32 v105, 0x1cd90, v105
	s_lshl_b32 s19, s36, 3
	s_add_i32 s19, s19, s8
	v_add_u32_e32 v94, s19, v96
	v_cmp_gt_i32_e64 s[4:5], s18, v94
	v_mov_b32_e32 v32, 0
	v_mov_b32_e32 v33, 0
	v_mov_b32_e32 v34, 0
	v_mov_b32_e32 v35, 0
	s_and_saveexec_b64 s[6:7], s[4:5]
	v_lshl_add_u32 v36, v94, 1, v94
	v_lshlrev_b32_e32 v36, 2, v36
	global_load_dwordx4 v[32:35], v36, s[10:11]
	s_mov_b64 exec, s[6:7]
	s_waitcnt vmcnt(6)
	ds_write_b128 v40, v[6:9]
	s_waitcnt vmcnt(5)
	ds_write_b128 v40, v[10:13] offset:4352
	s_waitcnt vmcnt(4)
	ds_write_b128 v41, v[14:17]
	s_waitcnt vmcnt(3)
	ds_write_b128 v41, v[18:21] offset:16384
	s_waitcnt vmcnt(2)
	ds_write_b128 v41, v[22:25] offset:32768
	s_waitcnt vmcnt(1)
	ds_write_b128 v41, v[26:29] offset:49152
	s_and_saveexec_b64 s[6:7], s[34:35]
	ds_write_b128 v38, v[42:45]
	s_mov_b64 exec, s[6:7]
	s_waitcnt vmcnt(0)
	v_sub_u32_e32 v72, v33, v32
	v_sub_u32_e32 v108, v34, v33
	v_sub_u32_e32 v35, v35, v34
	v_add_lshl_u32 v37, v32, v97, 2
	v_add_lshl_u32 v38, v33, v97, 2
	v_add_lshl_u32 v39, v34, v97, 2
	v_mov_b32_e32 v36, 0x4000000
	v_mov_b32_e32 v68, 0x4000000
	v_mov_b32_e32 v74, 0x4000000
	v_mov_b32_e32 v85, 0x4000000
	v_mov_b32_e32 v84, 0x4000000
	v_mov_b32_e32 v109, 0x4000000
	v_mov_b32_e32 v107, 0x4000000
	v_mov_b32_e32 v106, 0x4000000
	v_mov_b32_e32 v95, 0x4000000
	s_mov_b64 s[6:7], exec
	v_cmp_lt_i32_e32 vcc, v97, v72
	s_and_b64 exec, exec, vcc
	global_load_dword v36, v37, s[12:13]
	v_cmp_lt_i32_e32 vcc, v100, v72
	s_and_b64 exec, exec, vcc
	global_load_dword v68, v37, s[12:13] offset:32
	v_cmp_lt_i32_e32 vcc, v101, v72
	s_and_b64 exec, exec, vcc
	global_load_dword v74, v37, s[12:13] offset:64
	s_mov_b64 exec, s[6:7]
	v_cmp_lt_i32_e32 vcc, v97, v108
	s_and_b64 exec, exec, vcc
	global_load_dword v85, v38, s[12:13]
	v_cmp_lt_i32_e32 vcc, v100, v108
	s_and_b64 exec, exec, vcc
	global_load_dword v84, v38, s[12:13] offset:32
	v_cmp_lt_i32_e32 vcc, v101, v108
	s_and_b64 exec, exec, vcc
	global_load_dword v109, v38, s[12:13] offset:64
	s_mov_b64 exec, s[6:7]
	v_cmp_lt_i32_e32 vcc, v97, v35
	s_and_b64 exec, exec, vcc
	global_load_dword v107, v39, s[12:13]
	v_cmp_lt_i32_e32 vcc, v100, v35
	s_and_b64 exec, exec, vcc
	global_load_dword v106, v39, s[12:13] offset:32
	v_cmp_lt_i32_e32 vcc, v101, v35
	s_and_b64 exec, exec, vcc
	global_load_dword v95, v39, s[12:13] offset:64
	s_mov_b64 exec, s[6:7]
	s_waitcnt lgkmcnt(0)
	s_barrier
	s_cmp_ge_i32 s36, s9
	s_cbranch_scc1 .LBB4_103
	s_branch .Lp1_after_idx

.LBB4_101:
	s_or_b64 exec, exec, s[6:7]
	s_waitcnt lgkmcnt(0)
	ds_write_b128 v104, v[48:51]
	ds_read_b128 v[48:51], v105 offset:384
	ds_read_b128 v[52:55], v103
	ds_read_b128 v[56:59], v105 offset:9088
	s_waitcnt lgkmcnt(1)
	v_mfma_f32_16x16x32_f16 v[32:35], v[48:51], v[52:55], v[32:35]
	ds_read_b128 v[48:51], v105 offset:17792
	s_waitcnt lgkmcnt(1)
	v_mfma_f32_16x16x32_f16 v[36:39], v[56:59], v[52:55], v[36:39]
	s_waitcnt lgkmcnt(0)
	v_mfma_f32_16x16x32_f16 v[56:59], v[48:51], v[52:55], v[40:43]
	s_nop 2
	ds_read_b128 v[40:43], v105 offset:26496
	s_waitcnt lgkmcnt(0)
	v_mfma_f32_16x16x32_f16 v[50:53], v[40:43], v[52:55], v[44:47]
	ds_read_b128 v[40:43], v105 offset:448
	ds_read_b128 v[60:63], v103 offset:64
	ds_read_b128 v[64:67], v105 offset:9152
	v_add_u32_e32 v48, s19, v99
	v_cmp_gt_i32_e32 vcc, s18, v48
	s_and_b64 s[4:5], s[2:3], vcc
	s_waitcnt lgkmcnt(1)
	v_mfma_f32_16x16x32_f16 v[44:47], v[40:43], v[60:63], v[32:35]
	s_mov_b64 s[6:7], s[20:21]
	s_mov_b64 s[22:23], s[24:25]
	s_nop 0
	ds_read_b128 v[32:35], v105 offset:17856
	s_waitcnt lgkmcnt(1)
	v_mfma_f32_16x16x32_f16 v[40:43], v[64:67], v[60:63], v[36:39]
	ds_read_b128 v[64:67], v105 offset:26560
	s_waitcnt lgkmcnt(1)
	v_mfma_f32_16x16x32_f16 v[36:39], v[32:35], v[60:63], v[56:59]
	s_waitcnt lgkmcnt(0)
	v_mfma_f32_16x16x32_f16 v[32:35], v[64:67], v[60:63], v[50:53]
	s_and_saveexec_b64 s[22:23], s[4:5]
	s_xor_b64 s[4:5], exec, s[22:23]
	s_cbranch_execz .LBB4_15
	v_add_u32_e32 v50, 0x1cc90, v88
	ds_read_b128 v[52:55], v50
	ds_read_b128 v[56:59], v50 offset:16
	ds_read_b128 v[60:63], v50 offset:32
	ds_read_b128 v[64:67], v50 offset:48
	v_ashrrev_i32_e32 v49, 31, v48
	v_lshlrev_b64 v[68:69], 6, v[48:49]
	v_lshlrev_b64 v[70:71], 7, v[48:49]
	v_lshl_add_u64 v[68:69], v[92:93], 0, v[68:69]
	v_lshl_add_u64 v[70:71], v[90:91], 0, v[70:71]
	s_waitcnt lgkmcnt(3)
	v_add_f32_e32 v44, v44, v52
	v_add_f32_e32 v45, v45, v53
	v_add_f32_e32 v46, v46, v54
	v_add_f32_e32 v47, v47, v55
	v_max_f32_e32 v44, 0, v44
	v_max_f32_e32 v45, 0, v45
	v_max_f32_e32 v46, 0, v46
	v_max_f32_e32 v47, 0, v47
	v_mul_f32_e32 v52, 0x42800000, v44
	v_mul_f32_e32 v53, 0x42800000, v45
	v_mul_f32_e32 v54, 0x42800000, v46
	v_mul_f32_e32 v55, 0x42800000, v47
	v_min_f32_e32 v52, 0x43e00000, v52
	v_min_f32_e32 v53, 0x43e00000, v53
	v_min_f32_e32 v54, 0x43e00000, v54
	v_min_f32_e32 v55, 0x43e00000, v55
	v_cvt_pk_fp8_f32 v72, v52, v53
	v_cvt_pk_f16_f32 v76, v44, v45
	v_cvt_pk_fp8_f32 v72, v54, v55 op_sel:[0,0,1]
	v_cvt_pk_f16_f32 v77, v46, v47
	s_waitcnt lgkmcnt(2)
	v_add_f32_e32 v40, v40, v56
	v_add_f32_e32 v41, v41, v57
	v_add_f32_e32 v42, v42, v58
	v_add_f32_e32 v43, v43, v59
	v_max_f32_e32 v40, 0, v40
	v_max_f32_e32 v41, 0, v41
	v_max_f32_e32 v42, 0, v42
	v_max_f32_e32 v43, 0, v43
	v_mul_f32_e32 v56, 0x42800000, v40
	v_mul_f32_e32 v57, 0x42800000, v41
	v_mul_f32_e32 v58, 0x42800000, v42
	v_mul_f32_e32 v59, 0x42800000, v43
	v_min_f32_e32 v56, 0x43e00000, v56
	v_min_f32_e32 v57, 0x43e00000, v57
	v_min_f32_e32 v58, 0x43e00000, v58
	v_min_f32_e32 v59, 0x43e00000, v59
	v_cvt_pk_fp8_f32 v73, v56, v57
	v_cvt_pk_f16_f32 v78, v40, v41
	v_cvt_pk_fp8_f32 v73, v58, v59 op_sel:[0,0,1]
	v_cvt_pk_f16_f32 v79, v42, v43
	s_waitcnt lgkmcnt(1)
	v_add_f32_e32 v36, v36, v60
	v_add_f32_e32 v37, v37, v61
	v_add_f32_e32 v38, v38, v62
	v_add_f32_e32 v39, v39, v63
	v_max_f32_e32 v36, 0, v36
	v_max_f32_e32 v37, 0, v37
	v_max_f32_e32 v38, 0, v38
	v_max_f32_e32 v39, 0, v39
	v_mul_f32_e32 v60, 0x42800000, v36
	v_mul_f32_e32 v61, 0x42800000, v37
	v_mul_f32_e32 v62, 0x42800000, v38
	v_mul_f32_e32 v63, 0x42800000, v39
	v_min_f32_e32 v60, 0x43e00000, v60
	v_min_f32_e32 v61, 0x43e00000, v61
	v_min_f32_e32 v62, 0x43e00000, v62
	v_min_f32_e32 v63, 0x43e00000, v63
	v_cvt_pk_fp8_f32 v74, v60, v61
	v_cvt_pk_f16_f32 v80, v36, v37
	v_cvt_pk_fp8_f32 v74, v62, v63 op_sel:[0,0,1]
	v_cvt_pk_f16_f32 v81, v38, v39
	s_waitcnt lgkmcnt(0)
	v_add_f32_e32 v32, v32, v64
	v_add_f32_e32 v33, v33, v65
	v_add_f32_e32 v34, v34, v66
	v_add_f32_e32 v35, v35, v67
	v_max_f32_e32 v32, 0, v32
	v_max_f32_e32 v33, 0, v33
	v_max_f32_e32 v34, 0, v34
	v_max_f32_e32 v35, 0, v35
	v_mul_f32_e32 v64, 0x42800000, v32
	v_mul_f32_e32 v65, 0x42800000, v33
	v_mul_f32_e32 v66, 0x42800000, v34
	v_mul_f32_e32 v67, 0x42800000, v35
	v_min_f32_e32 v64, 0x43e00000, v64
	v_min_f32_e32 v65, 0x43e00000, v65
	v_min_f32_e32 v66, 0x43e00000, v66
	v_min_f32_e32 v67, 0x43e00000, v67
	v_cvt_pk_fp8_f32 v75, v64, v65
	v_cvt_pk_f16_f32 v82, v32, v33
	v_cvt_pk_fp8_f32 v75, v66, v67 op_sel:[0,0,1]
	v_cvt_pk_f16_f32 v83, v34, v35
	s_nop 0
	global_store_dwordx4 v[68:69], v[72:75], off
	global_store_dwordx4 v[70:71], v[76:79], off
	global_store_dwordx4 v[70:71], v[80:83], off offset:16
	s_branch .LBB4_15
